# v10 plus converter f32 weight loads as sc1 nt (bypass L1)
# baseline (speedup 1.0000x reference)
.Lcv_dec_done_1:
	global_load_dwordx4 v[2:5], v70, s[62:63] sc1 nt
	s_add_u32 s62, s62, s70
	s_addc_u32 s63, s63, 0
	global_load_dwordx4 v[6:9], v70, s[62:63] sc1 nt
	s_add_u32 s62, s62, s70
	s_addc_u32 s63, s63, 0
	global_load_dwordx4 v[10:13], v70, s[62:63] sc1 nt
	s_add_u32 s62, s62, s70
	s_addc_u32 s63, s63, 0
	global_load_dwordx4 v[14:17], v70, s[62:63] sc1 nt
	s_add_u32 s62, s62, s70
	s_addc_u32 s63, s63, 0
	global_load_dwordx4 v[18:21], v70, s[62:63] sc1 nt
	s_add_u32 s62, s62, s70
	s_addc_u32 s63, s63, 0
	global_load_dwordx4 v[22:25], v70, s[62:63] sc1 nt
	s_add_u32 s62, s62, s70
	s_addc_u32 s63, s63, 0
	global_load_dwordx4 v[26:29], v70, s[62:63] sc1 nt
	s_add_u32 s62, s62, s70
	s_addc_u32 s63, s63, 0
	global_load_dwordx4 v[30:33], v70, s[62:63] sc1 nt
	s_add_u32 s62, s62, s71
	s_addc_u32 s63, s63, 0
	global_load_dwordx4 v[34:37], v70, s[62:63] sc1 nt
	s_add_u32 s62, s62, s70
	s_addc_u32 s63, s63, 0
	global_load_dwordx4 v[38:41], v70, s[62:63] sc1 nt
	s_add_u32 s62, s62, s70
	s_addc_u32 s63, s63, 0
	global_load_dwordx4 v[42:45], v70, s[62:63] sc1 nt
	s_add_u32 s62, s62, s70
	s_addc_u32 s63, s63, 0
	global_load_dwordx4 v[46:49], v70, s[62:63] sc1 nt
	s_add_u32 s62, s62, s70
	s_addc_u32 s63, s63, 0
	global_load_dwordx4 v[50:53], v70, s[62:63] sc1 nt
	s_add_u32 s62, s62, s70
	s_addc_u32 s63, s63, 0
	global_load_dwordx4 v[54:57], v70, s[62:63] sc1 nt
	s_add_u32 s62, s62, s70
	s_addc_u32 s63, s63, 0
	global_load_dwordx4 v[58:61], v70, s[62:63] sc1 nt
	s_add_u32 s62, s62, s70
	s_addc_u32 s63, s63, 0
	global_load_dwordx4 v[62:65], v70, s[62:63] sc1 nt
	s_min_u32 s0, s30, 0x2fff
	s_add_u32 s30, s30, s31
	s_cmp_lt_u32 s0, 0x2000
	s_cbranch_scc0 .Lcv_w2_2
	s_lshr_b32 s1, s0, 8
	s_bfe_u32 s3, s0, 0x40004
	s_bfe_u32 s7, s0, 0x30001
	s_and_b32 s0, s0, 1
	s_lshl_b32 s6, s1, 25
	s_lshl_b32 s49, s3, 21
	s_add_u32 s6, s6, s49
	s_lshl_b32 s49, s34, 17
	s_add_u32 s6, s6, s49
	s_lshl_b32 s49, s0, 13
	s_add_u32 s6, s6, s49
	s_lshl_b32 s49, s7, 10
	s_add_u32 s6, s6, s49
	s_add_u32 s62, s8, s6
	s_addc_u32 s63, s9, 0
	s_lshl_b32 s6, s1, 23
	s_lshl_b32 s49, s7, 20
	s_add_u32 s6, s6, s49
	s_lshl_b32 s49, s0, 18
	s_add_u32 s6, s6, s49
	s_lshl_b32 s49, s3, 7
	s_add_u32 s6, s6, s49
	s_add_u32 s58, s12, s6
	s_addc_u32 s59, s13, 0
	s_mov_b32 s70, 0x4000
	s_mov_b32 s71, 0xe4000
	s_mov_b32 s87, 0x60000
	v_mov_b32_e32 v70, v68
	s_branch .Lcv_dec_done_2

.Lcv_dec_done_2:
	global_load_dwordx4 v[84:87], v70, s[62:63] sc1 nt
	s_add_u32 s62, s62, s70
	s_addc_u32 s63, s63, 0
	global_load_dwordx4 v[88:91], v70, s[62:63] sc1 nt
	s_add_u32 s62, s62, s70
	s_addc_u32 s63, s63, 0
	global_load_dwordx4 v[92:95], v70, s[62:63] sc1 nt
	s_add_u32 s62, s62, s70
	s_addc_u32 s63, s63, 0
	global_load_dwordx4 v[96:99], v70, s[62:63] sc1 nt
	s_add_u32 s62, s62, s70
	s_addc_u32 s63, s63, 0
	global_load_dwordx4 v[100:103], v70, s[62:63] sc1 nt
	s_add_u32 s62, s62, s70
	s_addc_u32 s63, s63, 0
	global_load_dwordx4 v[104:107], v70, s[62:63] sc1 nt
	s_add_u32 s62, s62, s70
	s_addc_u32 s63, s63, 0
	global_load_dwordx4 v[108:111], v70, s[62:63] sc1 nt
	s_add_u32 s62, s62, s70
	s_addc_u32 s63, s63, 0
	global_load_dwordx4 v[112:115], v70, s[62:63] sc1 nt
	s_add_u32 s62, s62, s71
	s_addc_u32 s63, s63, 0
	global_load_dwordx4 v[116:119], v70, s[62:63] sc1 nt
	s_add_u32 s62, s62, s70
	s_addc_u32 s63, s63, 0
	global_load_dwordx4 v[120:123], v70, s[62:63] sc1 nt
	s_add_u32 s62, s62, s70
	s_addc_u32 s63, s63, 0
	global_load_dwordx4 v[124:127], v70, s[62:63] sc1 nt
	s_add_u32 s62, s62, s70
	s_addc_u32 s63, s63, 0
	global_load_dwordx4 v[128:131], v70, s[62:63] sc1 nt
	s_add_u32 s62, s62, s70
	s_addc_u32 s63, s63, 0
	global_load_dwordx4 v[132:135], v70, s[62:63] sc1 nt
	s_add_u32 s62, s62, s70
	s_addc_u32 s63, s63, 0
	global_load_dwordx4 v[136:139], v70, s[62:63] sc1 nt
	s_add_u32 s62, s62, s70
	s_addc_u32 s63, s63, 0
	global_load_dwordx4 v[140:143], v70, s[62:63] sc1 nt
	s_add_u32 s62, s62, s70
	s_addc_u32 s63, s63, 0
	global_load_dwordx4 v[144:147], v70, s[62:63] sc1 nt
	s_waitcnt vmcnt(16)
	s_branch .Lcv_convA

.Lcv_dec_done_3:
	global_load_dwordx4 v[2:5], v70, s[62:63] sc1 nt
	s_add_u32 s62, s62, s70
	s_addc_u32 s63, s63, 0
	global_load_dwordx4 v[6:9], v70, s[62:63] sc1 nt
	s_add_u32 s62, s62, s70
	s_addc_u32 s63, s63, 0
	global_load_dwordx4 v[10:13], v70, s[62:63] sc1 nt
	s_add_u32 s62, s62, s70
	s_addc_u32 s63, s63, 0
	global_load_dwordx4 v[14:17], v70, s[62:63] sc1 nt
	s_add_u32 s62, s62, s70
	s_addc_u32 s63, s63, 0
	global_load_dwordx4 v[18:21], v70, s[62:63] sc1 nt
	s_add_u32 s62, s62, s70
	s_addc_u32 s63, s63, 0
	global_load_dwordx4 v[22:25], v70, s[62:63] sc1 nt
	s_add_u32 s62, s62, s70
	s_addc_u32 s63, s63, 0
	global_load_dwordx4 v[26:29], v70, s[62:63] sc1 nt
	s_add_u32 s62, s62, s70
	s_addc_u32 s63, s63, 0
	global_load_dwordx4 v[30:33], v70, s[62:63] sc1 nt
	s_add_u32 s62, s62, s71
	s_addc_u32 s63, s63, 0
	global_load_dwordx4 v[34:37], v70, s[62:63] sc1 nt
	s_add_u32 s62, s62, s70
	s_addc_u32 s63, s63, 0
	global_load_dwordx4 v[38:41], v70, s[62:63] sc1 nt
	s_add_u32 s62, s62, s70
	s_addc_u32 s63, s63, 0
	global_load_dwordx4 v[42:45], v70, s[62:63] sc1 nt
	s_add_u32 s62, s62, s70
	s_addc_u32 s63, s63, 0
	global_load_dwordx4 v[46:49], v70, s[62:63] sc1 nt
	s_add_u32 s62, s62, s70
	s_addc_u32 s63, s63, 0
	global_load_dwordx4 v[50:53], v70, s[62:63] sc1 nt
	s_add_u32 s62, s62, s70
	s_addc_u32 s63, s63, 0
	global_load_dwordx4 v[54:57], v70, s[62:63] sc1 nt
	s_add_u32 s62, s62, s70
	s_addc_u32 s63, s63, 0
	global_load_dwordx4 v[58:61], v70, s[62:63] sc1 nt
	s_add_u32 s62, s62, s70
	s_addc_u32 s63, s63, 0
	global_load_dwordx4 v[62:65], v70, s[62:63] sc1 nt

.Lcv_dec_done_4:
	global_load_dwordx4 v[84:87], v70, s[62:63] sc1 nt
	s_add_u32 s62, s62, s70
	s_addc_u32 s63, s63, 0
	global_load_dwordx4 v[88:91], v70, s[62:63] sc1 nt
	s_add_u32 s62, s62, s70
	s_addc_u32 s63, s63, 0
	global_load_dwordx4 v[92:95], v70, s[62:63] sc1 nt
	s_add_u32 s62, s62, s70
	s_addc_u32 s63, s63, 0
	global_load_dwordx4 v[96:99], v70, s[62:63] sc1 nt
	s_add_u32 s62, s62, s70
	s_addc_u32 s63, s63, 0
	global_load_dwordx4 v[100:103], v70, s[62:63] sc1 nt
	s_add_u32 s62, s62, s70
	s_addc_u32 s63, s63, 0
	global_load_dwordx4 v[104:107], v70, s[62:63] sc1 nt
	s_add_u32 s62, s62, s70
	s_addc_u32 s63, s63, 0
	global_load_dwordx4 v[108:111], v70, s[62:63] sc1 nt
	s_add_u32 s62, s62, s70
	s_addc_u32 s63, s63, 0
	global_load_dwordx4 v[112:115], v70, s[62:63] sc1 nt
	s_add_u32 s62, s62, s71
	s_addc_u32 s63, s63, 0
	global_load_dwordx4 v[116:119], v70, s[62:63] sc1 nt
	s_add_u32 s62, s62, s70
	s_addc_u32 s63, s63, 0
	global_load_dwordx4 v[120:123], v70, s[62:63] sc1 nt
	s_add_u32 s62, s62, s70
	s_addc_u32 s63, s63, 0
	global_load_dwordx4 v[124:127], v70, s[62:63] sc1 nt
	s_add_u32 s62, s62, s70
	s_addc_u32 s63, s63, 0
	global_load_dwordx4 v[128:131], v70, s[62:63] sc1 nt
	s_add_u32 s62, s62, s70
	s_addc_u32 s63, s63, 0
	global_load_dwordx4 v[132:135], v70, s[62:63] sc1 nt
	s_add_u32 s62, s62, s70
	s_addc_u32 s63, s63, 0
	global_load_dwordx4 v[136:139], v70, s[62:63] sc1 nt
	s_add_u32 s62, s62, s70
	s_addc_u32 s63, s63, 0
	global_load_dwordx4 v[140:143], v70, s[62:63] sc1 nt
	s_add_u32 s62, s62, s70
	s_addc_u32 s63, s63, 0
	global_load_dwordx4 v[144:147], v70, s[62:63] sc1 nt
	s_branch .Lcv_loopA
